# conv phase: the 12 input-row loads a wave makes per tile are issued together (one wait) instead of one at a time
# speedup vs baseline: 1.0085x; 1.0085x over previous
; #define GAS __attribute__((address_space(1)))
; #define LAS __attribute__((address_space(3)))
; #define NTLD(P) (NT_STREAMS ? __builtin_nontemporal_load(P) : *(P))
; __device__ __forceinline__ void phase_conv(Frame& F) {
;     ...
;     for (int ti = F.vcu; ti < 544; ti += F.G) {
;         int rowbase, L, p0;
;         if (ti < 512) { rowbase = (ti >> 6) * SEQ; p0 = (ti & 63) * 64; L = SEQ; } else { const int q = ti - 512; rowbase = TL + (q >> 2) * CTXL; p0 = (q & 3) * 64; L = CTXL; }
;         __syncthreads();
;         for (int rr = F.wave; rr < 94; rr += 8) { const int p = p0 - 15 + rr; v4u val = (v4u){0u, 0u, 0u, 0u};
;             if (p >= 0 && p < L) val = NTLD((const GAS v4u*)(AG + (size_t)(rowbase + p) * 512 + F.lane * 8));
;             *(LAS v4u*)(tile + rr * 512 + F.lane * 8) = val; }
;         __syncthreads();
.LBB0_347:
	s_andn2_b64 vcc, exec, s[2:3]
	s_cbranch_vccnz .LBB0_352
	s_and_b64 s[0:1], s[0:1], exec
	s_cselect_b32 s0, 0x1000, s46
	s_add_i32 s5, s10, s4
	v_mov_b32_e32 v22, v76
	s_mov_b32 s1, s44
	v_mov_b32_e32 v80, 0
	v_mov_b32_e32 v81, 0
	v_mov_b32_e32 v82, 0
	v_mov_b32_e32 v83, 0
	s_add_i32 s2, s4, s1
	s_cmp_ge_u32 s2, s0
	s_cbranch_scc1 .Lct_skip_0
	s_add_i32 s2, s5, s1
	s_ashr_i32 s3, s2, 31
	s_lshl_b64 s[2:3], s[2:3], 10
	v_lshl_add_u64 v[2:3], v[18:19], 0, s[2:3]
	global_load_dwordx4 v[80:83], v[2:3], off nt
.Lct_skip_0:
	s_add_i32 s1, s1, 8
	v_mov_b32_e32 v84, 0
	v_mov_b32_e32 v85, 0
	v_mov_b32_e32 v86, 0
	v_mov_b32_e32 v87, 0
	s_add_i32 s2, s4, s1
	s_cmp_ge_u32 s2, s0
	s_cbranch_scc1 .Lct_skip_1
	s_add_i32 s2, s5, s1
	s_ashr_i32 s3, s2, 31
	s_lshl_b64 s[2:3], s[2:3], 10
	v_lshl_add_u64 v[2:3], v[18:19], 0, s[2:3]
	global_load_dwordx4 v[84:87], v[2:3], off nt
.Lct_skip_1:
	s_add_i32 s1, s1, 8
	v_mov_b32_e32 v88, 0
	v_mov_b32_e32 v89, 0
	v_mov_b32_e32 v90, 0
	v_mov_b32_e32 v91, 0
	s_add_i32 s2, s4, s1
	s_cmp_ge_u32 s2, s0
	s_cbranch_scc1 .Lct_skip_2
	s_add_i32 s2, s5, s1
	s_ashr_i32 s3, s2, 31
	s_lshl_b64 s[2:3], s[2:3], 10
	v_lshl_add_u64 v[2:3], v[18:19], 0, s[2:3]
	global_load_dwordx4 v[88:91], v[2:3], off nt
.Lct_skip_2:
	s_add_i32 s1, s1, 8
	v_mov_b32_e32 v92, 0
	v_mov_b32_e32 v93, 0
	v_mov_b32_e32 v94, 0
	v_mov_b32_e32 v95, 0
	s_add_i32 s2, s4, s1
	s_cmp_ge_u32 s2, s0
	s_cbranch_scc1 .Lct_skip_3
	s_add_i32 s2, s5, s1
	s_ashr_i32 s3, s2, 31
	s_lshl_b64 s[2:3], s[2:3], 10
	v_lshl_add_u64 v[2:3], v[18:19], 0, s[2:3]
	global_load_dwordx4 v[92:95], v[2:3], off nt
.Lct_skip_3:
	s_add_i32 s1, s1, 8
	v_mov_b32_e32 v96, 0
	v_mov_b32_e32 v97, 0
	v_mov_b32_e32 v98, 0
	v_mov_b32_e32 v99, 0
	s_add_i32 s2, s4, s1
	s_cmp_ge_u32 s2, s0
	s_cbranch_scc1 .Lct_skip_4
	s_add_i32 s2, s5, s1
	s_ashr_i32 s3, s2, 31
	s_lshl_b64 s[2:3], s[2:3], 10
	v_lshl_add_u64 v[2:3], v[18:19], 0, s[2:3]
	global_load_dwordx4 v[96:99], v[2:3], off nt
.Lct_skip_4:
	s_add_i32 s1, s1, 8
	v_mov_b32_e32 v100, 0
	v_mov_b32_e32 v101, 0
	v_mov_b32_e32 v102, 0
	v_mov_b32_e32 v103, 0
	s_add_i32 s2, s4, s1
	s_cmp_ge_u32 s2, s0
	s_cbranch_scc1 .Lct_skip_5
	s_add_i32 s2, s5, s1
	s_ashr_i32 s3, s2, 31
	s_lshl_b64 s[2:3], s[2:3], 10
	v_lshl_add_u64 v[2:3], v[18:19], 0, s[2:3]
	global_load_dwordx4 v[100:103], v[2:3], off nt
.Lct_skip_5:
	s_add_i32 s1, s1, 8
	v_mov_b32_e32 v104, 0
	v_mov_b32_e32 v105, 0
	v_mov_b32_e32 v106, 0
	v_mov_b32_e32 v107, 0
	s_add_i32 s2, s4, s1
	s_cmp_ge_u32 s2, s0
	s_cbranch_scc1 .Lct_skip_6
	s_add_i32 s2, s5, s1
	s_ashr_i32 s3, s2, 31
	s_lshl_b64 s[2:3], s[2:3], 10
	v_lshl_add_u64 v[2:3], v[18:19], 0, s[2:3]
	global_load_dwordx4 v[104:107], v[2:3], off nt
.Lct_skip_6:
	s_add_i32 s1, s1, 8
	v_mov_b32_e32 v108, 0
	v_mov_b32_e32 v109, 0
	v_mov_b32_e32 v110, 0
	v_mov_b32_e32 v111, 0
	s_add_i32 s2, s4, s1
	s_cmp_ge_u32 s2, s0
	s_cbranch_scc1 .Lct_skip_7
	s_add_i32 s2, s5, s1
	s_ashr_i32 s3, s2, 31
	s_lshl_b64 s[2:3], s[2:3], 10
	v_lshl_add_u64 v[2:3], v[18:19], 0, s[2:3]
	global_load_dwordx4 v[108:111], v[2:3], off nt
.Lct_skip_7:
	s_add_i32 s1, s1, 8
	v_mov_b32_e32 v112, 0
	v_mov_b32_e32 v113, 0
	v_mov_b32_e32 v114, 0
	v_mov_b32_e32 v115, 0
	s_add_i32 s2, s4, s1
	s_cmp_ge_u32 s2, s0
	s_cbranch_scc1 .Lct_skip_8
	s_add_i32 s2, s5, s1
	s_ashr_i32 s3, s2, 31
	s_lshl_b64 s[2:3], s[2:3], 10
	v_lshl_add_u64 v[2:3], v[18:19], 0, s[2:3]
	global_load_dwordx4 v[112:115], v[2:3], off nt
.Lct_skip_8:
	s_add_i32 s1, s1, 8
	v_mov_b32_e32 v116, 0
	v_mov_b32_e32 v117, 0
	v_mov_b32_e32 v118, 0
	v_mov_b32_e32 v119, 0
	s_add_i32 s2, s4, s1
	s_cmp_ge_u32 s2, s0
	s_cbranch_scc1 .Lct_skip_9
	s_add_i32 s2, s5, s1
	s_ashr_i32 s3, s2, 31
	s_lshl_b64 s[2:3], s[2:3], 10
	v_lshl_add_u64 v[2:3], v[18:19], 0, s[2:3]
	global_load_dwordx4 v[116:119], v[2:3], off nt
.Lct_skip_9:
	s_add_i32 s1, s1, 8
	v_mov_b32_e32 v120, 0
	v_mov_b32_e32 v121, 0
	v_mov_b32_e32 v122, 0
	v_mov_b32_e32 v123, 0
	s_add_i32 s2, s4, s1
	s_cmp_ge_u32 s2, s0
	s_cbranch_scc1 .Lct_skip_10
	s_add_i32 s2, s5, s1
	s_ashr_i32 s3, s2, 31
	s_lshl_b64 s[2:3], s[2:3], 10
	v_lshl_add_u64 v[2:3], v[18:19], 0, s[2:3]
	global_load_dwordx4 v[120:123], v[2:3], off nt
.Lct_skip_10:
	s_add_i32 s1, s1, 8
	s_cmpk_gt_i32 s1, 0x4e
	s_cbranch_scc1 .Lct_ld_done
	v_mov_b32_e32 v124, 0
	v_mov_b32_e32 v125, 0
	v_mov_b32_e32 v126, 0
	v_mov_b32_e32 v127, 0
	s_add_i32 s2, s4, s1
	s_cmp_ge_u32 s2, s0
	s_cbranch_scc1 .Lct_skip_11
	s_add_i32 s2, s5, s1
	s_ashr_i32 s3, s2, 31
	s_lshl_b64 s[2:3], s[2:3], 10
	v_lshl_add_u64 v[2:3], v[18:19], 0, s[2:3]
	global_load_dwordx4 v[124:127], v[2:3], off nt
.Lct_skip_11:
	s_add_i32 s1, s1, 8
.Lct_ld_done:
	s_waitcnt vmcnt(0)
	ds_write_b128 v22, v[80:83]
	v_add_u32_e32 v22, 0x2000, v22
	ds_write_b128 v22, v[84:87]
	v_add_u32_e32 v22, 0x2000, v22
	ds_write_b128 v22, v[88:91]
	v_add_u32_e32 v22, 0x2000, v22
	ds_write_b128 v22, v[92:95]
	v_add_u32_e32 v22, 0x2000, v22
	ds_write_b128 v22, v[96:99]
	v_add_u32_e32 v22, 0x2000, v22
	ds_write_b128 v22, v[100:103]
	v_add_u32_e32 v22, 0x2000, v22
	ds_write_b128 v22, v[104:107]
	v_add_u32_e32 v22, 0x2000, v22
	ds_write_b128 v22, v[108:111]
	v_add_u32_e32 v22, 0x2000, v22
	ds_write_b128 v22, v[112:115]
	v_add_u32_e32 v22, 0x2000, v22
	ds_write_b128 v22, v[116:119]
	v_add_u32_e32 v22, 0x2000, v22
	ds_write_b128 v22, v[120:123]
	v_add_u32_e32 v22, 0x2000, v22
	s_cmpk_lt_i32 s1, 0x51
	s_cbranch_scc1 .Lct_wr_done
	ds_write_b128 v22, v[124:127]
	v_add_u32_e32 v22, 0x2000, v22
.Lct_wr_done:
.LBB0_352:
	v_mad_i64_i32 v[2:3], s[0:1], s5, v77, v[20:21]
	s_mov_b64 s[38:39], 0
	v_mov_b32_e32 v100, v69
	s_waitcnt lgkmcnt(0)
	s_barrier
